# all three latent attention key loops: lead half QK MFMAs first then LDS reads and DMA issue; lag half DMA (and V reads where registers allow) before softmax; dead m0 saves removed
# baseline (speedup 1.0000x reference)
; #define ATT_SB() __builtin_amdgcn_sched_barrier(0)
; #define ATT_DMA_K(t, sl) do { glds16(ksrc + (size_t)(t) * 64 * kpitch, (unsigned)__builtin_amdgcn_readfirstlane(kdst + (sl) * KSLOT)); \
;         if constexpr (DQK == 96) glds16(krsrc + (size_t)(t) * 64 * 32, (unsigned)__builtin_amdgcn_readfirstlane(krdst + (sl) * KSLOT)); } while (0)
; #define ATT_DMA_V(t, sl) do { glds16(vsrc + (size_t)(t) * 64, (unsigned)__builtin_amdgcn_readfirstlane(vdst + (sl) * VSLOT)); \
;         if constexpr (DV == 128) glds16(vsrc + (size_t)64 * NR + (size_t)(t) * 64, (unsigned)__builtin_amdgcn_readfirstlane(vdst + (sl) * VSLOT + 8192)); } while (0)
; #define ATT_KLOAD(sl) do { _Pragma("unroll") for (int kb_ = 0; kb_ < NKW; ++kb_) _Pragma("unroll") for (int ds_ = 0; ds_ < NDS; ++ds_) { \
;         if (ds_ < 2) kf[kb_ * NDS + ds_] = *(const LAS bf16x8*)(kp[ds_ & 1] + (sl) * KSLOT + (kb_ & 1) * 512 + (kb_ >> 1) * 4096); \
;         else kf[kb_ * NDS + ds_] = *(const LAS bf16x8*)(krp + (sl) * KSLOT + (kb_ & 1) * 256 + (kb_ >> 1) * 2048); } } while (0)
; template <int DQK, int DV, bool LEAD> ...
;     ...
;         __builtin_amdgcn_s_waitcnt(0xC07F);
;         if constexpr (!LEAD) { ATT_EXP(); ATT_SUMPACK(); ATT_SB(); }
;         ATT_VLOAD(s_prev, 0); ATT_SB();
;         { const int tk = (t + 3 < NT) ? t + 3 : NT - 1; ATT_DMA_K(tk, s_cur); }
;         { const int tv = (t + 1 < NT) ? t + 1 : NT - 1; ATT_DMA_V(tv, s_next); }
;         ATT_SB();
;         if constexpr (LEAD) {
;             ATT_QK(); ATT_SB();
;             ATT_PVP(0); ATT_SB();
;             if constexpr (DV == 128) { ATT_VLOAD(s_prev, 1); ATT_SB(); ATT_EXP(); ATT_SB(); ATT_PVP(1); ATT_SB(); }
;             if (one_) ATT_KLOAD(s_next);
;             ATT_SB();
;             if constexpr (DV == 64) ATT_EXP();
;             ATT_SUMPACK();
;             asm volatile("" : "+v"(pw[0]), "+v"(pw[1]), "+v"(pw[2]), "+v"(pw[3]));
; #pragma unroll
;             for (int qb = 0; qb < NQB; ++qb) asm volatile("" : "+v"(lsum[qb]));
;         } else {
;             if constexpr (DV == 128) {
;                 ATT_PVP(0); ATT_SB();
;                 ATT_VLOAD(s_prev, 1); ATT_SB();
;                 ATT_QK(); ATT_SB();
.LBB0_941:
	s_mov_b32 s5, s47
	s_mov_b32 s47, s38
	s_add_i32 s38, s48, -1
	s_min_u32 s38, s38, 0x80
	s_mul_i32 s38, s38, 0x38000
	v_lshl_add_u64 v[162:163], v[204:205], 0, s[38:39]
	s_lshl_b32 s38, s5, 13
	s_add_i32 s38, s38, s43
	v_lshl_add_u64 v[162:163], v[162:163], 0, s[96:97]
	s_mov_b32 m0, s38
	s_nop 0
	global_load_lds_dwordx4 v[162:163], off
	s_min_u32 s38, s48, 0x83
	s_lshl_b32 s38, s38, 7
	s_lshl_b32 s49, s47, 14
	v_lshl_add_u64 v[162:163], v[206:207], 0, s[38:39]
	s_add_i32 s49, s49, s16
	s_mov_b32 m0, s49
	s_nop 0
	global_load_lds_dwordx4 v[162:163], off
	v_lshl_add_u64 v[162:163], v[208:209], 0, s[38:39]
	s_add_i32 s38, s49, 0x2000
	s_mov_b32 m0, s38
	s_nop 0
	global_load_lds_dwordx4 v[162:163], off
	v_exp_f32_e32 v138, v138
	v_exp_f32_e32 v139, v139
	v_exp_f32_e32 v140, v140
	v_exp_f32_e32 v141, v141
	v_exp_f32_e32 v126, v126
	v_exp_f32_e32 v127, v127
	v_exp_f32_e32 v128, v128
	v_exp_f32_e32 v129, v129
	v_exp_f32_e32 v122, v122
	v_exp_f32_e32 v114, v114
	v_add_f32_e32 v146, v138, v139
	v_add_f32_e32 v147, v140, v141
	v_exp_f32_e32 v123, v123
	v_exp_f32_e32 v115, v115
	v_add_f32_e32 v146, v146, v147
	v_add_f32_e32 v147, v126, v127
	v_add_f32_e32 v148, v128, v129
	v_add_f32_e32 v147, v147, v148
	v_exp_f32_e32 v124, v124
	v_exp_f32_e32 v116, v116
	v_add_f32_e32 v146, v122, v146
	v_add_f32_e32 v147, v114, v147
	s_waitcnt lgkmcnt(0)
	v_exp_f32_e32 v125, v125
	v_exp_f32_e32 v117, v117
	v_add_f32_e32 v146, v123, v146
	v_add_f32_e32 v147, v115, v147
	v_exp_f32_e32 v130, v130
	v_exp_f32_e32 v118, v118
	v_add_f32_e32 v146, v124, v146
	v_add_f32_e32 v147, v116, v147
	v_exp_f32_e32 v131, v131
	v_exp_f32_e32 v119, v119
	v_add_f32_e32 v146, v125, v146
	v_add_f32_e32 v147, v117, v147
	v_exp_f32_e32 v132, v132
	v_exp_f32_e32 v120, v120
	v_add_f32_e32 v146, v130, v146
	v_add_f32_e32 v147, v118, v147
	v_exp_f32_e32 v133, v133
	v_exp_f32_e32 v121, v121
	v_add_f32_e32 v146, v131, v146
	v_add_f32_e32 v147, v119, v147
	v_exp_f32_e32 v142, v142
	v_exp_f32_e32 v134, v134
	v_add_f32_e32 v146, v132, v146
	v_add_f32_e32 v147, v120, v147
	v_exp_f32_e32 v143, v143
	v_exp_f32_e32 v135, v135
	v_add_f32_e32 v146, v133, v146
	v_add_f32_e32 v147, v121, v147
	v_exp_f32_e32 v144, v144
	v_exp_f32_e32 v136, v136
	v_add_f32_e32 v146, v142, v146
	v_add_f32_e32 v147, v134, v147
	v_exp_f32_e32 v145, v145
	v_exp_f32_e32 v137, v137
	v_add_f32_e32 v146, v143, v146
	v_add_f32_e32 v147, v135, v147
	v_add_f32_e32 v146, v144, v146
	v_add_f32_e32 v147, v136, v147
	v_add_f32_e32 v213, v145, v146
	v_add_f32_e32 v212, v137, v147
	v_cvt_pk_bf16_f32 v146, v138, v139
	v_cvt_pk_bf16_f32 v147, v140, v141
	v_cvt_pk_bf16_f32 v148, v122, v123
	v_cvt_pk_bf16_f32 v149, v124, v125
	v_cvt_pk_bf16_f32 v150, v126, v127
	v_cvt_pk_bf16_f32 v151, v128, v129
	v_cvt_pk_bf16_f32 v152, v114, v115
	v_cvt_pk_bf16_f32 v153, v116, v117
	v_cvt_pk_bf16_f32 v154, v130, v131
	v_cvt_pk_bf16_f32 v155, v132, v133
	v_cvt_pk_bf16_f32 v156, v142, v143
	v_cvt_pk_bf16_f32 v157, v144, v145
	v_cvt_pk_bf16_f32 v158, v118, v119
	v_cvt_pk_bf16_f32 v159, v120, v121
	v_cvt_pk_bf16_f32 v160, v134, v135
	v_cvt_pk_bf16_f32 v161, v136, v137
	s_lshl_b32 s49, s4, 14
	v_add_u32_e32 v164, s49, v218
	v_add_u32_e32 v166, s49, v219
	ds_read_b128 v[114:117], v164 offset:36864
	ds_read_b128 v[118:121], v164 offset:38912
	ds_read_b128 v[122:125], v166 offset:36864
	ds_read_b128 v[126:129], v166 offset:38912
	ds_read_b128 v[130:133], v164 offset:40960
	ds_read_b128 v[134:137], v164 offset:43008
	ds_read_b128 v[138:141], v166 offset:40960
	ds_read_b128 v[142:145], v166 offset:43008
	s_waitcnt lgkmcnt(7)
	v_mfma_f32_16x16x32_bf16 v[78:81], v[114:117], v[146:149], v[78:81]
	v_mfma_f32_16x16x32_bf16 v[74:77], v[114:117], v[150:153], v[74:77]
	s_waitcnt lgkmcnt(6)
	v_mfma_f32_16x16x32_bf16 v[70:73], v[118:121], v[146:149], v[70:73]
	v_mfma_f32_16x16x32_bf16 v[62:65], v[118:121], v[150:153], v[62:65]
	s_waitcnt lgkmcnt(3)
	v_mfma_f32_16x16x32_bf16 v[54:57], v[130:133], v[146:149], v[54:57]
	v_mfma_f32_16x16x32_bf16 v[50:53], v[130:133], v[150:153], v[50:53]
	s_waitcnt lgkmcnt(2)
	v_mfma_f32_16x16x32_bf16 v[46:49], v[134:137], v[146:149], v[46:49]
	v_mfma_f32_16x16x32_bf16 v[42:45], v[134:137], v[150:153], v[42:45]
	v_mfma_f32_16x16x32_bf16 v[78:81], v[122:125], v[154:157], v[78:81]
	v_mfma_f32_16x16x32_bf16 v[74:77], v[122:125], v[158:161], v[74:77]
	v_mfma_f32_16x16x32_bf16 v[70:73], v[126:129], v[154:157], v[70:73]
	v_mfma_f32_16x16x32_bf16 v[62:65], v[126:129], v[158:161], v[62:65]
	s_waitcnt lgkmcnt(1)
	v_mfma_f32_16x16x32_bf16 v[54:57], v[138:141], v[154:157], v[54:57]
	v_mfma_f32_16x16x32_bf16 v[50:53], v[138:141], v[158:161], v[50:53]
	s_waitcnt lgkmcnt(0)
	v_mfma_f32_16x16x32_bf16 v[46:49], v[142:145], v[154:157], v[46:49]
	v_mfma_f32_16x16x32_bf16 v[42:45], v[142:145], v[158:161], v[42:45]
	ds_read_b128 v[186:189], v164 offset:45056
	ds_read_b128 v[174:177], v164 offset:47104
	ds_read_b128 v[190:193], v166 offset:45056
	ds_read_b128 v[178:181], v166 offset:47104
	ds_read_b128 v[170:173], v164 offset:49152
	ds_read_b128 v[162:165], v164 offset:51200
	ds_read_b128 v[182:185], v166 offset:49152
	ds_read_b128 v[166:169], v166 offset:51200
	v_mfma_f32_16x16x32_bf16 v[114:117], v[82:85], v[10:13], 0
	v_mfma_f32_16x16x32_bf16 v[118:121], v[82:85], v[58:61], 0
	v_mfma_f32_16x16x32_bf16 v[138:141], v[90:93], v[2:5], v[114:117]
	v_mfma_f32_16x16x32_bf16 v[126:129], v[90:93], v[66:69], v[118:121]
	v_mfma_f32_16x16x32_bf16 v[114:117], v[86:89], v[10:13], 0
	v_mfma_f32_16x16x32_bf16 v[118:121], v[86:89], v[58:61], 0
	v_mfma_f32_16x16x32_bf16 v[122:125], v[94:97], v[2:5], v[114:117]
	v_mfma_f32_16x16x32_bf16 v[114:117], v[94:97], v[66:69], v[118:121]
	v_mfma_f32_16x16x32_bf16 v[118:121], v[98:101], v[10:13], 0
	v_mfma_f32_16x16x32_bf16 v[134:137], v[98:101], v[58:61], 0
	v_mfma_f32_16x16x32_bf16 v[130:133], v[106:109], v[2:5], v[118:121]
	v_mfma_f32_16x16x32_bf16 v[118:121], v[106:109], v[66:69], v[134:137]
	v_mfma_f32_16x16x32_bf16 v[134:137], v[102:105], v[10:13], 0
	v_mfma_f32_16x16x32_bf16 v[236:239], v[102:105], v[58:61], 0
	v_mfma_f32_16x16x32_bf16 v[142:145], v[110:113], v[2:5], v[134:137]
	v_mfma_f32_16x16x32_bf16 v[134:137], v[110:113], v[66:69], v[236:239]
	s_andn2_b64 vcc, exec, s[6:7]
	s_cbranch_vccnz .LBB0_943
; #define ATT_SB() __builtin_amdgcn_sched_barrier(0)
; #define ATT_KLOAD(sl) do { _Pragma("unroll") for (int kb_ = 0; kb_ < NKW; ++kb_) _Pragma("unroll") for (int ds_ = 0; ds_ < NDS; ++ds_) { \
;         if (ds_ < 2) kf[kb_ * NDS + ds_] = *(const LAS bf16x8*)(kp[ds_ & 1] + (sl) * KSLOT + (kb_ & 1) * 512 + (kb_ >> 1) * 4096); \
;         else kf[kb_ * NDS + ds_] = *(const LAS bf16x8*)(krp + (sl) * KSLOT + (kb_ & 1) * 256 + (kb_ >> 1) * 2048); } } while (0)
; #define ATT_QK() do { _Pragma("unroll") for (int kb_ = 0; kb_ < NKW; ++kb_) _Pragma("unroll") for (int ds_ = 0; ds_ < NDS; ++ds_) _Pragma("unroll") for (int qb_ = 0; qb_ < NQB; ++qb_) \
;         c[kb_][qb_] = __builtin_amdgcn_mfma_f32_16x16x32_bf16(kf[kb_ * NDS + ds_], qf[qb_ * NDS + ds_], ds_ == 0 ? zero4 : c[kb_][qb_], 0, 0, 0); } while (0)
; #define ATT_VLOAD(sl, h_) do { _Pragma("unroll") for (int g_ = 0; g_ < NVF; ++g_) { \
;         if constexpr (KS) vf[g_] = *(const LAS bf16x8*)(vpk + (sl) * VSLOT + g_ * 2048); \
;         else vf[g_] = *(const LAS bf16x8*)(vp[g_ & 1] + (sl) * VSLOT + ((h_) * 4 + (g_ >> 1)) * 2048); } } while (0)
; #define ATT_PVP(h_) do { _Pragma("unroll") for (int g_ = 0; g_ < NVF; ++g_) _Pragma("unroll") for (int qb_ = 0; qb_ < NQB; ++qb_) { \
;         const int db_ = KS ? g_ : (h_) * 4 + (g_ >> 1), sq_ = KS ? 0 : (g_ & 1); \
;         o[db_][qb_] = __builtin_amdgcn_mfma_f32_16x16x32_bf16(vf[g_], __builtin_bit_cast(bf16x8, pw[sq_ * NQB + qb_]), o[db_][qb_], 0, 0, 0); } } while (0)
; template <int DQK, int DV, bool LEAD> ...
;     ...
;             if constexpr (DV == 128) {
;                 ATT_PVP(0); ATT_SB();
;                 ATT_VLOAD(s_prev, 1); ATT_SB();
;                 ATT_QK(); ATT_SB();
;                 if (one_) { ATT_KLOAD(s_next); ATT_SB(); ATT_PVP(1); }
;                 ATT_SB();
	s_lshl_b32 s38, s47, 13
	v_add_u32_e32 v102, s38, v194
	v_add_u32_e32 v110, s38, v220
	ds_read_b128 v[82:85], v102
	ds_read_b128 v[86:89], v102 offset:512
	ds_read_b128 v[90:93], v110
	ds_read_b128 v[94:97], v110 offset:512
	ds_read_b128 v[98:101], v102 offset:4096
	ds_read_b128 v[102:105], v102 offset:4608
	ds_read_b128 v[106:109], v110 offset:4096
	ds_read_b128 v[110:113], v110 offset:4608
	s_waitcnt lgkmcnt(14)
	v_mfma_f32_16x16x32_bf16 v[38:41], v[186:189], v[146:149], v[38:41]
	v_mfma_f32_16x16x32_bf16 v[34:37], v[186:189], v[150:153], v[34:37]
	v_mfma_f32_16x16x32_bf16 v[30:33], v[174:177], v[146:149], v[30:33]
	v_mfma_f32_16x16x32_bf16 v[26:29], v[174:177], v[150:153], v[26:29]
	s_waitcnt lgkmcnt(11)
	v_mfma_f32_16x16x32_bf16 v[22:25], v[170:173], v[146:149], v[22:25]
	v_mfma_f32_16x16x32_bf16 v[18:21], v[170:173], v[150:153], v[18:21]
	s_waitcnt lgkmcnt(10)
	v_mfma_f32_16x16x32_bf16 v[14:17], v[162:165], v[146:149], v[14:17]
	v_mfma_f32_16x16x32_bf16 v[6:9], v[162:165], v[150:153], v[6:9]
	v_mfma_f32_16x16x32_bf16 v[38:41], v[190:193], v[154:157], v[38:41]
	v_mfma_f32_16x16x32_bf16 v[34:37], v[190:193], v[158:161], v[34:37]
	v_mfma_f32_16x16x32_bf16 v[30:33], v[178:181], v[154:157], v[30:33]
	v_mfma_f32_16x16x32_bf16 v[26:29], v[178:181], v[158:161], v[26:29]
	s_waitcnt lgkmcnt(9)
	v_mfma_f32_16x16x32_bf16 v[22:25], v[182:185], v[154:157], v[22:25]
	v_mfma_f32_16x16x32_bf16 v[18:21], v[182:185], v[158:161], v[18:21]
	s_waitcnt lgkmcnt(8)
	v_mfma_f32_16x16x32_bf16 v[14:17], v[166:169], v[154:157], v[14:17]
	v_mfma_f32_16x16x32_bf16 v[6:9], v[166:169], v[158:161], v[6:9]

; #define ATT_SB() __builtin_amdgcn_sched_barrier(0)
; #define ATT_DMA_K(t, sl) do { glds16(ksrc + (size_t)(t) * 64 * kpitch, (unsigned)__builtin_amdgcn_readfirstlane(kdst + (sl) * KSLOT)); \
;         if constexpr (DQK == 96) glds16(krsrc + (size_t)(t) * 64 * 32, (unsigned)__builtin_amdgcn_readfirstlane(krdst + (sl) * KSLOT)); } while (0)
; #define ATT_DMA_V(t, sl) do { glds16(vsrc + (size_t)(t) * 64, (unsigned)__builtin_amdgcn_readfirstlane(vdst + (sl) * VSLOT)); \
;         if constexpr (DV == 128) glds16(vsrc + (size_t)64 * NR + (size_t)(t) * 64, (unsigned)__builtin_amdgcn_readfirstlane(vdst + (sl) * VSLOT + 8192)); } while (0)
; #define ATT_KLOAD(sl) do { _Pragma("unroll") for (int kb_ = 0; kb_ < NKW; ++kb_) _Pragma("unroll") for (int ds_ = 0; ds_ < NDS; ++ds_) { \
;         if (ds_ < 2) kf[kb_ * NDS + ds_] = *(const LAS bf16x8*)(kp[ds_ & 1] + (sl) * KSLOT + (kb_ & 1) * 512 + (kb_ >> 1) * 4096); \
;         else kf[kb_ * NDS + ds_] = *(const LAS bf16x8*)(krp + (sl) * KSLOT + (kb_ & 1) * 256 + (kb_ >> 1) * 2048); } } while (0)
; #define ATT_QK() do { _Pragma("unroll") for (int kb_ = 0; kb_ < NKW; ++kb_) _Pragma("unroll") for (int ds_ = 0; ds_ < NDS; ++ds_) _Pragma("unroll") for (int qb_ = 0; qb_ < NQB; ++qb_) \
;         c[kb_][qb_] = __builtin_amdgcn_mfma_f32_16x16x32_bf16(kf[kb_ * NDS + ds_], qf[qb_ * NDS + ds_], ds_ == 0 ? zero4 : c[kb_][qb_], 0, 0, 0); } while (0)
; #define ATT_VLOAD(sl, h_) do { _Pragma("unroll") for (int g_ = 0; g_ < NVF; ++g_) { \
;         if constexpr (KS) vf[g_] = *(const LAS bf16x8*)(vpk + (sl) * VSLOT + g_ * 2048); \
;         else vf[g_] = *(const LAS bf16x8*)(vp[g_ & 1] + (sl) * VSLOT + ((h_) * 4 + (g_ >> 1)) * 2048); } } while (0)
; template <int DQK, int DV, bool LEAD> ...
;     ...
;         ATT_VLOAD(s_prev, 0); ATT_SB();
;         { const int tk = (t + 3 < NT) ? t + 3 : NT - 1; ATT_DMA_K(tk, s_cur); }
;         { const int tv = (t + 1 < NT) ? t + 1 : NT - 1; ATT_DMA_V(tv, s_next); }
;         ATT_SB();
;         if constexpr (LEAD) {
;             ATT_QK(); ATT_SB();
;             ATT_PVP(0); ATT_SB();
;             if constexpr (DV == 128) { ATT_VLOAD(s_prev, 1); ATT_SB(); ATT_EXP(); ATT_SB(); ATT_PVP(1); ATT_SB(); }
;             if (one_) ATT_KLOAD(s_next);
;             ATT_SB();
.LBB0_948:
	v_mfma_f32_16x16x32_bf16 v[130:133], v[34:37], v[6:9], 0
	v_mfma_f32_16x16x32_bf16 v[134:137], v[34:37], v[10:13], 0
	v_mfma_f32_16x16x32_bf16 v[158:161], v[46:49], v[2:5], v[130:133]
	v_mfma_f32_16x16x32_bf16 v[130:133], v[38:41], v[6:9], 0
	v_mfma_f32_16x16x32_bf16 v[154:157], v[46:49], v[14:17], v[134:137]
	v_mfma_f32_16x16x32_bf16 v[134:137], v[38:41], v[10:13], 0
	v_mfma_f32_16x16x32_bf16 v[150:153], v[50:53], v[2:5], v[130:133]
	v_mfma_f32_16x16x32_bf16 v[130:133], v[54:57], v[6:9], 0
	v_mfma_f32_16x16x32_bf16 v[146:149], v[50:53], v[14:17], v[134:137]
	v_mfma_f32_16x16x32_bf16 v[134:137], v[54:57], v[10:13], 0
	v_mfma_f32_16x16x32_bf16 v[142:145], v[66:69], v[2:5], v[130:133]
	v_mfma_f32_16x16x32_bf16 v[130:133], v[62:65], v[6:9], 0
	v_mfma_f32_16x16x32_bf16 v[240:243], v[62:65], v[10:13], 0
	v_mfma_f32_16x16x32_bf16 v[138:141], v[66:69], v[14:17], v[134:137]
	v_mfma_f32_16x16x32_bf16 v[134:137], v[70:73], v[2:5], v[130:133]
	v_mfma_f32_16x16x32_bf16 v[130:133], v[70:73], v[14:17], v[240:243]
	s_lshl_b32 s29, s28, 14
	v_add_u32_e32 v179, s29, v178
	v_add_u32_e32 v192, s29, v177
	ds_read_b128 v[180:183], v179 offset:36864
	ds_read_b128 v[184:187], v179 offset:38912
	ds_read_b128 v[188:191], v192 offset:36864
	ds_read_b128 v[204:207], v192 offset:38912
	ds_read_b128 v[208:211], v179 offset:40960
	ds_read_b128 v[212:215], v179 offset:43008
	ds_read_b128 v[216:219], v192 offset:40960
	ds_read_b128 v[236:239], v192 offset:43008
	s_mov_b32 s29, s25
	s_mov_b32 s25, s30
	s_add_i32 s30, s16, -1
	s_min_u32 s30, s30, 0x80
	s_mul_i32 s38, s30, 0x38000
	s_lshl_b32 s30, s29, 13
	v_lshl_add_u64 v[252:253], v[162:163], 0, s[38:39]
	s_add_i32 s30, s30, s31
	v_lshl_add_u64 v[252:253], v[252:253], 0, s[96:97]
	s_mov_b32 m0, s30
	s_nop 0
	global_load_lds_dwordx4 v[252:253], off
	s_min_u32 s30, s16, 0x83
	s_lshl_b32 s38, s30, 7
	s_lshl_b32 s30, s25, 14
	v_lshl_add_u64 v[252:253], v[164:165], 0, s[38:39]
	s_add_i32 s30, s30, s40
	s_mov_b32 m0, s30
	s_nop 0
	global_load_lds_dwordx4 v[252:253], off
	v_lshl_add_u64 v[252:253], v[166:167], 0, s[38:39]
	s_addk_i32 s30, 0x2000
	s_mov_b32 m0, s30
	s_nop 0
	global_load_lds_dwordx4 v[252:253], off
	s_waitcnt lgkmcnt(7)
	v_mfma_f32_16x16x32_bf16 v[126:129], v[180:183], v[82:85], v[126:129]
	v_mfma_f32_16x16x32_bf16 v[122:125], v[180:183], v[94:97], v[122:125]
	s_waitcnt lgkmcnt(6)
	v_mfma_f32_16x16x32_bf16 v[118:121], v[184:187], v[82:85], v[118:121]
	v_mfma_f32_16x16x32_bf16 v[114:117], v[184:187], v[94:97], v[114:117]
	s_waitcnt lgkmcnt(3)
	v_mfma_f32_16x16x32_bf16 v[110:113], v[208:211], v[82:85], v[110:113]
	v_mfma_f32_16x16x32_bf16 v[106:109], v[208:211], v[94:97], v[106:109]
	s_waitcnt lgkmcnt(2)
	v_mfma_f32_16x16x32_bf16 v[90:93], v[212:215], v[82:85], v[90:93]
	v_mfma_f32_16x16x32_bf16 v[86:89], v[212:215], v[94:97], v[86:89]
	v_mfma_f32_16x16x32_bf16 v[126:129], v[188:191], v[98:101], v[126:129]
	v_mfma_f32_16x16x32_bf16 v[122:125], v[188:191], v[102:105], v[122:125]
	v_mfma_f32_16x16x32_bf16 v[118:121], v[204:207], v[98:101], v[118:121]
	v_mfma_f32_16x16x32_bf16 v[114:117], v[204:207], v[102:105], v[114:117]
	s_waitcnt lgkmcnt(1)
	v_mfma_f32_16x16x32_bf16 v[110:113], v[216:219], v[98:101], v[110:113]
	v_mfma_f32_16x16x32_bf16 v[106:109], v[216:219], v[102:105], v[106:109]
	s_waitcnt lgkmcnt(0)
	v_mfma_f32_16x16x32_bf16 v[90:93], v[236:239], v[98:101], v[90:93]
	v_mfma_f32_16x16x32_bf16 v[86:89], v[236:239], v[102:105], v[86:89]
	ds_read_b128 v[180:183], v179 offset:45056
	ds_read_b128 v[184:187], v179 offset:47104
	ds_read_b128 v[188:191], v192 offset:45056
	ds_read_b128 v[204:207], v192 offset:47104
	ds_read_b128 v[208:211], v179 offset:49152
	ds_read_b128 v[212:215], v179 offset:51200
	ds_read_b128 v[216:219], v192 offset:49152
	ds_read_b128 v[236:239], v192 offset:51200
	s_waitcnt lgkmcnt(7)
	v_mfma_f32_16x16x32_bf16 v[78:81], v[180:183], v[82:85], v[78:81]
	v_mfma_f32_16x16x32_bf16 v[74:77], v[180:183], v[94:97], v[74:77]
	s_waitcnt lgkmcnt(6)
	v_mfma_f32_16x16x32_bf16 v[58:61], v[184:187], v[82:85], v[58:61]
	v_mfma_f32_16x16x32_bf16 v[42:45], v[184:187], v[94:97], v[42:45]
	s_waitcnt lgkmcnt(3)
	v_mfma_f32_16x16x32_bf16 v[30:33], v[208:211], v[82:85], v[30:33]
	v_mfma_f32_16x16x32_bf16 v[26:29], v[208:211], v[94:97], v[26:29]
	s_waitcnt lgkmcnt(2)
	v_mfma_f32_16x16x32_bf16 v[22:25], v[212:215], v[82:85], v[22:25]
	v_mfma_f32_16x16x32_bf16 v[18:21], v[212:215], v[94:97], v[18:21]
	v_mfma_f32_16x16x32_bf16 v[78:81], v[188:191], v[98:101], v[78:81]
	v_mfma_f32_16x16x32_bf16 v[74:77], v[188:191], v[102:105], v[74:77]
	v_mfma_f32_16x16x32_bf16 v[58:61], v[204:207], v[98:101], v[58:61]
	v_mfma_f32_16x16x32_bf16 v[42:45], v[204:207], v[102:105], v[42:45]
	s_waitcnt lgkmcnt(1)
	v_mfma_f32_16x16x32_bf16 v[30:33], v[216:219], v[98:101], v[30:33]
	v_mfma_f32_16x16x32_bf16 v[26:29], v[216:219], v[102:105], v[26:29]
	s_waitcnt lgkmcnt(0)
	v_mfma_f32_16x16x32_bf16 v[22:25], v[236:239], v[98:101], v[22:25]
	v_mfma_f32_16x16x32_bf16 v[18:21], v[236:239], v[102:105], v[18:21]
	s_andn2_b64 vcc, exec, s[4:5]
	s_cbranch_vccnz .LBB0_950
	s_lshl_b32 s30, s25, 13
	v_add_u32_e32 v62, s30, v173
	v_add_u32_e32 v70, s30, v176
	ds_read_b128 v[34:37], v62
	ds_read_b128 v[38:41], v62 offset:512
	ds_read_b128 v[46:49], v70
	ds_read_b128 v[50:53], v70 offset:512
	ds_read_b128 v[54:57], v62 offset:4096
	ds_read_b128 v[62:65], v62 offset:4608
	ds_read_b128 v[66:69], v70 offset:4096
	ds_read_b128 v[70:73], v70 offset:4608

; #define ATT_SB() __builtin_amdgcn_sched_barrier(0)
; #define ATT_DMA_K(t, sl) do { glds16(ksrc + (size_t)(t) * 64 * kpitch, (unsigned)__builtin_amdgcn_readfirstlane(kdst + (sl) * KSLOT)); \
;         if constexpr (DQK == 96) glds16(krsrc + (size_t)(t) * 64 * 32, (unsigned)__builtin_amdgcn_readfirstlane(krdst + (sl) * KSLOT)); } while (0)
; #define ATT_DMA_V(t, sl) do { glds16(vsrc + (size_t)(t) * 64, (unsigned)__builtin_amdgcn_readfirstlane(vdst + (sl) * VSLOT)); \
;         if constexpr (DV == 128) glds16(vsrc + (size_t)64 * NR + (size_t)(t) * 64, (unsigned)__builtin_amdgcn_readfirstlane(vdst + (sl) * VSLOT + 8192)); } while (0)
; template <int DQK, int DV, bool LEAD> ...
;     ...
;         __builtin_amdgcn_s_waitcnt(0xC07F);
;         if constexpr (!LEAD) { ATT_EXP(); ATT_SUMPACK(); ATT_SB(); }
;         ATT_VLOAD(s_prev, 0); ATT_SB();
;         { const int tk = (t + 3 < NT) ? t + 3 : NT - 1; ATT_DMA_K(tk, s_cur); }
;         { const int tv = (t + 1 < NT) ? t + 1 : NT - 1; ATT_DMA_V(tv, s_next); }
;         ATT_SB();
;         if constexpr (LEAD) {
;             ATT_QK(); ATT_SB();
;             ATT_PVP(0); ATT_SB();
;             if constexpr (DV == 128) { ATT_VLOAD(s_prev, 1); ATT_SB(); ATT_EXP(); ATT_SB(); ATT_PVP(1); ATT_SB(); }
;             if (one_) ATT_KLOAD(s_next);
;             ATT_SB();
;             if constexpr (DV == 64) ATT_EXP();
;             ATT_SUMPACK();
;             asm volatile("" : "+v"(pw[0]), "+v"(pw[1]), "+v"(pw[2]), "+v"(pw[3]));
; #pragma unroll
;             for (int qb = 0; qb < NQB; ++qb) asm volatile("" : "+v"(lsum[qb]));
;         } else {
;             if constexpr (DV == 128) {
;                 ATT_PVP(0); ATT_SB();
;                 ATT_VLOAD(s_prev, 1); ATT_SB();
;                 ATT_QK(); ATT_SB();
;                 if (one_) { ATT_KLOAD(s_next); ATT_SB(); ATT_PVP(1); }
;                 ATT_SB();
;             } else {
;                 __builtin_amdgcn_s_setprio(1);
;                 ATT_QK(); ATT_SB();
;                 if (one_) { ATT_KLOAD(s_next); ATT_SB(); ATT_PVP(0); }
;                 ATT_SB();
;                 __builtin_amdgcn_s_setprio(0);
;             }
.LBB0_957:
	s_mov_b32 s5, s51
	s_mov_b32 s51, s38
	s_add_i32 s38, s16, -1
	v_lshl_add_u32 v170, s4, 13, v175
	ds_read_b128 v[160:163], v170 offset:36864
	ds_read_b128 v[156:159], v170 offset:38912
	ds_read_b128 v[152:155], v170 offset:40960
	ds_read_b128 v[148:151], v170 offset:43008
	s_min_u32 s38, s38, 0x80
	s_mul_i32 s38, s38, 0x38000
	s_lshl_b32 s52, s5, 13
	v_lshl_add_u64 v[172:173], v[164:165], 0, s[38:39]
	s_add_i32 s38, s52, s50
	v_lshl_add_u64 v[172:173], v[172:173], 0, s[96:97]
	s_mov_b32 m0, s38
	s_nop 0
	global_load_lds_dwordx4 v[172:173], off
	s_min_u32 s38, s16, 0x83
	s_lshl_b32 s38, s38, 7
	v_lshl_add_u64 v[172:173], v[166:167], 0, s[38:39]
	s_lshl_b32 s38, s51, 13
	s_add_i32 s53, s38, s45
	s_mov_b32 m0, s53
	s_nop 0
	global_load_lds_dwordx4 v[172:173], off
	v_exp_f32_e32 v177, v144
	v_exp_f32_e32 v178, v145
	v_exp_f32_e32 v179, v146
	v_exp_f32_e32 v180, v147
	v_exp_f32_e32 v181, v140
	v_exp_f32_e32 v182, v141
	v_exp_f32_e32 v183, v142
	v_exp_f32_e32 v184, v143
	v_exp_f32_e32 v185, v128
	v_exp_f32_e32 v186, v129
	v_exp_f32_e32 v188, v130
	v_exp_f32_e32 v190, v131
	v_exp_f32_e32 v193, v116
	v_exp_f32_e32 v194, v117
	v_exp_f32_e32 v204, v118
	v_exp_f32_e32 v206, v119
	v_add_f32_e32 v116, v177, v178
	v_add_f32_e32 v117, v179, v180
	v_exp_f32_e32 v187, v136
	v_exp_f32_e32 v203, v132
	v_exp_f32_e32 v197, v124
	v_exp_f32_e32 v212, v120
	v_add_f32_e32 v116, v116, v117
	v_add_f32_e32 v117, v181, v182
	v_add_f32_e32 v118, v183, v184
	v_add_f32_e32 v117, v117, v118
	v_add_f32_e32 v118, v185, v186
	v_add_f32_e32 v119, v188, v190
	v_exp_f32_e32 v189, v137
	v_exp_f32_e32 v205, v133
	v_exp_f32_e32 v209, v125
	v_exp_f32_e32 v213, v121
	v_add_f32_e32 v118, v118, v119
	v_add_f32_e32 v119, v193, v194
	v_add_f32_e32 v120, v204, v206
	v_add_f32_e32 v119, v119, v120
	v_exp_f32_e32 v191, v138
	v_exp_f32_e32 v207, v134
	v_exp_f32_e32 v210, v126
	v_exp_f32_e32 v214, v122
	v_add_f32_e32 v116, v187, v116
	v_add_f32_e32 v117, v203, v117
	v_add_f32_e32 v118, v197, v118
	v_add_f32_e32 v119, v212, v119
	s_waitcnt lgkmcnt(0)
	v_exp_f32_e32 v192, v139
	v_exp_f32_e32 v208, v135
	v_exp_f32_e32 v211, v127
	v_exp_f32_e32 v215, v123
	v_add_f32_e32 v116, v189, v116
	v_add_f32_e32 v117, v205, v117
	v_add_f32_e32 v118, v209, v118
	v_add_f32_e32 v119, v213, v119
	v_add_f32_e32 v116, v191, v116
	v_add_f32_e32 v117, v207, v117
	v_add_f32_e32 v118, v210, v118
	v_add_f32_e32 v119, v214, v119
	s_nop 0
	v_add_f32_e32 v173, v192, v116
	v_add_f32_e32 v172, v208, v117
	v_add_f32_e32 v171, v211, v118
	v_add_f32_e32 v170, v215, v119
	s_setprio 1
	v_mfma_f32_16x16x32_bf16 v[120:123], v[100:103], v[24:27], 0
	v_mfma_f32_16x16x32_bf16 v[124:127], v[100:103], v[56:59], 0
	v_mfma_f32_16x16x32_bf16 v[116:119], v[100:103], v[6:9], 0
	v_mfma_f32_16x16x32_bf16 v[132:135], v[100:103], v[76:79], 0
	v_mfma_f32_16x16x32_bf16 v[140:143], v[104:107], v[10:13], v[120:123]
	v_mfma_f32_16x16x32_bf16 v[128:131], v[104:107], v[60:63], v[124:127]
	v_mfma_f32_16x16x32_bf16 v[120:123], v[108:111], v[6:9], 0
	v_mfma_f32_16x16x32_bf16 v[124:127], v[108:111], v[24:27], 0
	v_mfma_f32_16x16x32_bf16 v[216:219], v[108:111], v[56:59], 0
	v_mfma_f32_16x16x32_bf16 v[236:239], v[108:111], v[76:79], 0
	v_mfma_f32_16x16x32_bf16 v[144:147], v[104:107], v[2:5], v[116:119]
	v_mfma_f32_16x16x32_bf16 v[116:119], v[104:107], v[84:87], v[132:135]
	v_mfma_f32_16x16x32_bf16 v[136:139], v[112:115], v[2:5], v[120:123]
	v_mfma_f32_16x16x32_bf16 v[132:135], v[112:115], v[10:13], v[124:127]
	v_mfma_f32_16x16x32_bf16 v[124:127], v[112:115], v[60:63], v[216:219]
	v_mfma_f32_16x16x32_bf16 v[120:123], v[112:115], v[84:87], v[236:239]
	s_andn2_b64 vcc, exec, s[6:7]
	s_cbranch_vccnz .LBB0_959
	v_add_u32_e32 v108, s38, v174
	v_add_u32_e32 v112, s38, v176
	ds_read_b128 v[100:103], v108
	ds_read_b128 v[104:107], v112
	ds_read_b128 v[108:111], v108 offset:512
	ds_read_b128 v[112:115], v112 offset:512
	v_cvt_pk_bf16_f32 v215, v214, v215
	v_cvt_pk_bf16_f32 v214, v212, v213
	v_cvt_pk_bf16_f32 v213, v204, v206
	v_cvt_pk_bf16_f32 v212, v193, v194
	v_cvt_pk_bf16_f32 v219, v210, v211
	v_cvt_pk_bf16_f32 v218, v197, v209
	v_cvt_pk_bf16_f32 v217, v188, v190
	v_cvt_pk_bf16_f32 v216, v185, v186
	v_cvt_pk_bf16_f32 v207, v207, v208
	v_cvt_pk_bf16_f32 v206, v203, v205
	v_cvt_pk_bf16_f32 v205, v183, v184
	v_cvt_pk_bf16_f32 v204, v181, v182
	v_cvt_pk_bf16_f32 v183, v191, v192
	v_cvt_pk_bf16_f32 v182, v187, v189
	v_cvt_pk_bf16_f32 v181, v179, v180
	v_cvt_pk_bf16_f32 v180, v177, v178
	s_waitcnt lgkmcnt(7)
	s_nop 0
	v_mfma_f32_16x16x32_bf16 v[96:99], v[160:163], v[180:183], v[96:99]
	v_mfma_f32_16x16x32_bf16 v[92:95], v[160:163], v[204:207], v[92:95]
	v_mfma_f32_16x16x32_bf16 v[88:91], v[160:163], v[216:219], v[88:91]
	v_mfma_f32_16x16x32_bf16 v[80:83], v[160:163], v[212:215], v[80:83]
	s_waitcnt lgkmcnt(6)
	v_mfma_f32_16x16x32_bf16 v[72:75], v[156:159], v[180:183], v[72:75]
	v_mfma_f32_16x16x32_bf16 v[68:71], v[156:159], v[204:207], v[68:71]
	v_mfma_f32_16x16x32_bf16 v[64:67], v[156:159], v[216:219], v[64:67]
	v_mfma_f32_16x16x32_bf16 v[52:55], v[156:159], v[212:215], v[52:55]
	s_waitcnt lgkmcnt(5)
	v_mfma_f32_16x16x32_bf16 v[48:51], v[152:155], v[180:183], v[48:51]
	v_mfma_f32_16x16x32_bf16 v[44:47], v[152:155], v[204:207], v[44:47]
	v_mfma_f32_16x16x32_bf16 v[40:43], v[152:155], v[216:219], v[40:43]
	v_mfma_f32_16x16x32_bf16 v[36:39], v[152:155], v[212:215], v[36:39]
	s_waitcnt lgkmcnt(4)
	v_mfma_f32_16x16x32_bf16 v[32:35], v[148:151], v[180:183], v[32:35]
	v_mfma_f32_16x16x32_bf16 v[28:31], v[148:151], v[204:207], v[28:31]
	v_mfma_f32_16x16x32_bf16 v[18:21], v[148:151], v[216:219], v[18:21]
	v_mfma_f32_16x16x32_bf16 v[14:17], v[148:151], v[212:215], v[14:17]

; #define ATT_SB() __builtin_amdgcn_sched_barrier(0)
; #define ATT_DMA_K(t, sl) do { glds16(ksrc + (size_t)(t) * 64 * kpitch, (unsigned)__builtin_amdgcn_readfirstlane(kdst + (sl) * KSLOT)); \
;         if constexpr (DQK == 96) glds16(krsrc + (size_t)(t) * 64 * 32, (unsigned)__builtin_amdgcn_readfirstlane(krdst + (sl) * KSLOT)); } while (0)
; #define ATT_DMA_V(t, sl) do { glds16(vsrc + (size_t)(t) * 64, (unsigned)__builtin_amdgcn_readfirstlane(vdst + (sl) * VSLOT)); \
;         if constexpr (DV == 128) glds16(vsrc + (size_t)64 * NR + (size_t)(t) * 64, (unsigned)__builtin_amdgcn_readfirstlane(vdst + (sl) * VSLOT + 8192)); } while (0)
; #define ATT_KLOAD(sl) do { _Pragma("unroll") for (int kb_ = 0; kb_ < NKW; ++kb_) _Pragma("unroll") for (int ds_ = 0; ds_ < NDS; ++ds_) { \
;         if (ds_ < 2) kf[kb_ * NDS + ds_] = *(const LAS bf16x8*)(kp[ds_ & 1] + (sl) * KSLOT + (kb_ & 1) * 512 + (kb_ >> 1) * 4096); \
;         else kf[kb_ * NDS + ds_] = *(const LAS bf16x8*)(krp + (sl) * KSLOT + (kb_ & 1) * 256 + (kb_ >> 1) * 2048); } } while (0)
; #define ATT_QK() do { _Pragma("unroll") for (int kb_ = 0; kb_ < NKW; ++kb_) _Pragma("unroll") for (int ds_ = 0; ds_ < NDS; ++ds_) _Pragma("unroll") for (int qb_ = 0; qb_ < NQB; ++qb_) \
;         c[kb_][qb_] = __builtin_amdgcn_mfma_f32_16x16x32_bf16(kf[kb_ * NDS + ds_], qf[qb_ * NDS + ds_], ds_ == 0 ? zero4 : c[kb_][qb_], 0, 0, 0); } while (0)
; template <int DQK, int DV, bool LEAD> ...
;     ...
;         ATT_VLOAD(s_prev, 0); ATT_SB();
;         { const int tk = (t + 3 < NT) ? t + 3 : NT - 1; ATT_DMA_K(tk, s_cur); }
;         { const int tv = (t + 1 < NT) ? t + 1 : NT - 1; ATT_DMA_V(tv, s_next); }
;         ATT_SB();
;         if constexpr (LEAD) {
;             ATT_QK(); ATT_SB();
;             ATT_PVP(0); ATT_SB();
;             if constexpr (DV == 128) { ATT_VLOAD(s_prev, 1); ATT_SB(); ATT_EXP(); ATT_SB(); ATT_PVP(1); ATT_SB(); }
;             if (one_) ATT_KLOAD(s_next);
;             ATT_SB();
;             if constexpr (DV == 64) ATT_EXP();
;             ATT_SUMPACK();
;             asm volatile("" : "+v"(pw[0]), "+v"(pw[1]), "+v"(pw[2]), "+v"(pw[3]));
; #pragma unroll
;             for (int qb = 0; qb < NQB; ++qb) asm volatile("" : "+v"(lsum[qb]));
.LBB0_965:
	v_mfma_f32_16x16x32_bf16 v[130:133], v[34:37], v[6:9], 0
	v_mfma_f32_16x16x32_bf16 v[134:137], v[34:37], v[14:17], 0
	v_mfma_f32_16x16x32_bf16 v[138:141], v[34:37], v[22:25], 0
	v_mfma_f32_16x16x32_bf16 v[142:145], v[34:37], v[26:29], 0
	v_mfma_f32_16x16x32_bf16 v[158:161], v[42:45], v[2:5], v[130:133]
	v_mfma_f32_16x16x32_bf16 v[154:157], v[42:45], v[10:13], v[134:137]
	v_mfma_f32_16x16x32_bf16 v[130:133], v[38:41], v[6:9], 0
	v_mfma_f32_16x16x32_bf16 v[134:137], v[38:41], v[14:17], 0
	v_mfma_f32_16x16x32_bf16 v[208:211], v[38:41], v[22:25], 0
	v_mfma_f32_16x16x32_bf16 v[212:215], v[38:41], v[26:29], 0
	v_mfma_f32_16x16x32_bf16 v[150:153], v[42:45], v[18:21], v[138:141]
	v_mfma_f32_16x16x32_bf16 v[142:145], v[42:45], v[30:33], v[142:145]
	v_mfma_f32_16x16x32_bf16 v[146:149], v[46:49], v[2:5], v[130:133]
	v_mfma_f32_16x16x32_bf16 v[138:141], v[46:49], v[10:13], v[134:137]
	v_mfma_f32_16x16x32_bf16 v[134:137], v[46:49], v[18:21], v[208:211]
	v_mfma_f32_16x16x32_bf16 v[130:133], v[46:49], v[30:33], v[212:215]
	v_lshl_add_u32 v254, s29, 13, v177
	ds_read_b128 v[180:183], v254 offset:36864
	ds_read_b128 v[184:187], v254 offset:38912
	ds_read_b128 v[188:191], v254 offset:40960
	ds_read_b128 v[204:207], v254 offset:43008
	s_mov_b32 s40, s28
	s_mov_b32 s28, s37
	s_add_i32 s16, s27, -1
	s_min_u32 s16, s16, 0x80
	s_mul_i32 s38, s16, 0x38000
	s_lshl_b32 s16, s40, 13
	v_lshl_add_u64 v[252:253], v[162:163], 0, s[38:39]
	s_add_i32 s37, s16, s49
	v_lshl_add_u64 v[252:253], v[252:253], 0, s[96:97]
	s_mov_b32 m0, s37
	s_nop 0
	global_load_lds_dwordx4 v[252:253], off
	s_min_u32 s37, s27, 0x83
	s_lshl_b32 s38, s37, 7
	s_lshl_b32 s37, s28, 13
	v_lshl_add_u64 v[252:253], v[164:165], 0, s[38:39]
	s_add_i32 s38, s37, s36
	s_mov_b32 m0, s38
	s_nop 0
	global_load_lds_dwordx4 v[252:253], off
	s_waitcnt lgkmcnt(3)
	v_mfma_f32_16x16x32_bf16 v[118:121], v[180:183], v[102:105], v[118:121]
	v_mfma_f32_16x16x32_bf16 v[110:113], v[180:183], v[114:117], v[110:113]
	v_mfma_f32_16x16x32_bf16 v[106:109], v[180:183], v[122:125], v[106:109]
	v_mfma_f32_16x16x32_bf16 v[98:101], v[180:183], v[126:129], v[98:101]
	s_waitcnt lgkmcnt(2)
	v_mfma_f32_16x16x32_bf16 v[94:97], v[184:187], v[102:105], v[94:97]
	v_mfma_f32_16x16x32_bf16 v[90:93], v[184:187], v[114:117], v[90:93]
	v_mfma_f32_16x16x32_bf16 v[86:89], v[184:187], v[122:125], v[86:89]
	v_mfma_f32_16x16x32_bf16 v[82:85], v[184:187], v[126:129], v[82:85]
	s_waitcnt lgkmcnt(1)
	v_mfma_f32_16x16x32_bf16 v[78:81], v[188:191], v[102:105], v[78:81]
	v_mfma_f32_16x16x32_bf16 v[74:77], v[188:191], v[114:117], v[74:77]
	v_mfma_f32_16x16x32_bf16 v[70:73], v[188:191], v[122:125], v[70:73]
	v_mfma_f32_16x16x32_bf16 v[66:69], v[188:191], v[126:129], v[66:69]
	s_waitcnt lgkmcnt(0)
	v_mfma_f32_16x16x32_bf16 v[62:65], v[204:207], v[102:105], v[62:65]
	v_mfma_f32_16x16x32_bf16 v[58:61], v[204:207], v[114:117], v[58:61]
	v_mfma_f32_16x16x32_bf16 v[54:57], v[204:207], v[122:125], v[54:57]
	v_mfma_f32_16x16x32_bf16 v[50:53], v[204:207], v[126:129], v[50:53]
	s_andn2_b64 vcc, exec, s[4:5]
	s_cbranch_vccnz .LBB0_964
	v_add_u32_e32 v38, s37, v175
	v_add_u32_e32 v46, s37, v178
	ds_read_b128 v[34:37], v38
	ds_read_b128 v[38:41], v38 offset:512
	ds_read_b128 v[42:45], v46
	ds_read_b128 v[46:49], v46 offset:512
	s_branch .LBB0_964
